# stack E plus: the diff-attention own-queue pop for the next unit issued at the start of the current unit and consumed at the next loop top
# speedup vs baseline: 1.0054x; 1.0042x over previous
.LBB0_551:
	s_add_u32 s2, s16, s0
	s_addc_u32 s3, s17, s1
	global_load_dwordx4 v[6:9], v4, s[2:3]
	global_load_dwordx4 v[10:13], v4, s[2:3] offset:16
	s_add_u32 s2, s18, s0
	s_addc_u32 s3, s19, s1
	global_load_dwordx4 v[14:17], v4, s[2:3]
	global_load_dwordx4 v[18:21], v4, s[2:3] offset:16
	s_add_u32 s2, s8, s0
	s_addc_u32 s3, s9, s1
	global_load_dwordx4 v[22:25], v4, s[2:3]
	global_load_dwordx4 v[26:29], v4, s[2:3] offset:16
	s_add_u32 s2, s10, s0
	s_addc_u32 s3, s11, s1
	global_load_dwordx4 v[30:33], v4, s[2:3]
	global_load_dwordx4 v[34:37], v4, s[2:3] offset:16
	s_add_u32 s0, s0, 32
	s_addc_u32 s1, s1, 0
	s_cmpk_eq_i32 s0, 0x100
	s_waitcnt vmcnt(7)
	v_mov_b32_e32 v38, v6
	v_mov_b32_e32 v6, v8
	s_waitcnt vmcnt(6)
	v_mov_b32_e32 v8, v10
	v_mov_b32_e32 v10, v12
	s_waitcnt vmcnt(5)
	v_mov_b32_e32 v12, v14
	v_mov_b32_e32 v14, v16
	s_waitcnt vmcnt(3)
	v_mov_b32_e32 v39, v22
	v_mov_b32_e32 v22, v7
	v_mov_b32_e32 v7, v24
	v_mov_b32_e32 v24, v9
	s_waitcnt vmcnt(2)
	v_mov_b32_e32 v9, v26
	v_mov_b32_e32 v26, v11
	v_mov_b32_e32 v11, v28
	v_mov_b32_e32 v28, v13
	s_waitcnt vmcnt(1)
	v_mov_b32_e32 v13, v30
	v_mov_b32_e32 v30, v15
	v_pk_fma_f32 v[2:3], v[38:39], v[12:13], v[2:3]
	v_mov_b32_e32 v15, v32
	v_pk_fma_f32 v[2:3], v[22:23], v[30:31], v[2:3]
	v_mov_b32_e32 v32, v17
	v_pk_fma_f32 v[2:3], v[6:7], v[14:15], v[2:3]
	v_mov_b32_e32 v16, v18
	s_waitcnt vmcnt(0)
	v_mov_b32_e32 v17, v34
	v_pk_fma_f32 v[2:3], v[24:25], v[32:33], v[2:3]
	v_mov_b32_e32 v34, v19
	v_pk_fma_f32 v[2:3], v[8:9], v[16:17], v[2:3]
	v_mov_b32_e32 v18, v20
	v_mov_b32_e32 v19, v36
	v_pk_fma_f32 v[2:3], v[26:27], v[34:35], v[2:3]
	v_mov_b32_e32 v36, v21
	v_pk_fma_f32 v[2:3], v[10:11], v[18:19], v[2:3]
	s_nop 0
	v_pk_fma_f32 v[2:3], v[28:29], v[36:37], v[2:3]
	s_cbranch_scc0 .LBB0_551
	v_mul_f32_e32 v1, 0x3fb8aa3b, v2
	s_mov_b32 s80, 0x3fb8aa3b
	v_rndne_f32_e32 v4, v1
	v_sub_f32_e32 v5, v1, v4
	v_fma_f32 v1, v2, s80, -v1
	v_fmac_f32_e32 v1, 0x32a5705f, v2
	v_add_f32_e32 v1, v5, v1
	v_exp_f32_e32 v1, v1
	v_cvt_i32_f32_e32 v4, v4
	s_mov_b32 s0, 0xc2ce8ed0
	v_cmp_ngt_f32_e32 vcc, s0, v2
	s_mov_b32 s1, 0x42b17218
	v_ldexp_f32 v1, v1, v4
	v_mul_f32_e32 v4, 0x3fb8aa3b, v3
	v_rndne_f32_e32 v5, v4
	v_sub_f32_e32 v6, v4, v5
	v_fma_f32 v4, v3, s80, -v4
	v_fmac_f32_e32 v4, 0x32a5705f, v3
	v_add_f32_e32 v4, v6, v4
	v_exp_f32_e32 v4, v4
	v_cvt_i32_f32_e32 v5, v5
	v_cndmask_b32_e32 v1, 0, v1, vcc
	v_mov_b32_e32 v6, 0x7f800000
	v_cmp_nlt_f32_e32 vcc, s1, v2
	s_add_u32 s44, s92, 0x3d000
	s_addc_u32 s45, s93, 0
	v_cndmask_b32_e32 v1, v6, v1, vcc
	v_cmp_ngt_f32_e32 vcc, s0, v3
	s_lshl_b32 s0, s81, 6
	v_ldexp_f32 v2, v4, v5
	s_add_u32 s0, s44, s0
	v_cndmask_b32_e32 v2, 0, v2, vcc
	v_cmp_nlt_f32_e32 vcc, s1, v3
	s_addc_u32 s1, s45, 0
	s_bfe_u32 s2, s90, 0x20003
	v_writelane_b32 v254, s0, 61
	s_cmp_lg_u32 s2, 0
	v_cndmask_b32_e32 v2, v6, v2, vcc
	v_writelane_b32 v254, s1, 62
	s_cselect_b64 s[0:1], -1, 0
	v_sub_f32_e32 v1, v1, v2
	v_writelane_b32 v254, s0, 63
	v_add_f32_e32 v188, 0x3e4ccccd, v1
	v_add_u32_e32 v1, -1, v0
	v_writelane_b32 v255, s1, 0
	v_readlane_b32 s0, v254, 49
	v_cmp_gt_u32_e64 s[6:7], 7, v1
	v_add_lshl_u32 v1, s90, v0, 6
	s_andn2_b32 s0, s0, 63
	v_and_b32_e32 v2, 0x1c0, v1
	v_mov_b32_e32 v3, 0
	v_or_b32_e32 v1, s0, v251
	v_readlane_b32 s0, v254, 50
	v_lshl_add_u64 v[190:191], s[44:45], 0, v[2:3]
	s_lshl_b32 s0, s0, 4
	v_lshrrev_b32_e32 v2, 2, v0
	v_and_b32_e32 v194, 60, v142
	v_and_or_b32 v192, v2, 12, s0
	v_mul_u32_u24_e32 v2, 33, v194
	v_lshrrev_b32_e32 v193, 4, v251
	v_lshlrev_b32_e32 v2, 2, v2
	s_add_i32 s0, s0, 0
	v_lshlrev_b32_e32 v4, 2, v193
	v_add3_u32 v195, s0, v2, v4
	v_ashrrev_i32_e32 v4, 3, v1
	v_add_u32_e32 v1, 0x200, v1
	s_movk_i32 s5, 0x880
	v_ashrrev_i32_e32 v1, 3, v1
	v_cmp_lt_u32_e32 vcc, 18, v0
	v_mad_i64_i32 v[196:197], s[0:1], v4, s5, 0
	v_mad_i64_i32 v[198:199], s[0:1], v1, s5, 0
	s_movk_i32 s70, 0x80
	v_cndmask_b32_e64 v5, 0, 1, vcc
	v_cmp_lt_u32_e32 vcc, 26, v0
	v_cmp_gt_u32_e64 s[0:1], s70, v0
	s_movk_i32 s4, 0x84
	v_cndmask_b32_e64 v6, 0, 1, vcc
	v_cmp_lt_u32_e32 vcc, 34, v0
	v_writelane_b32 v255, s0, 1
	v_mul_lo_u32 v203, v4, s4
	v_cndmask_b32_e64 v7, 0, 1, vcc
	v_cmp_lt_u32_e32 vcc, 45, v0
	v_writelane_b32 v255, s1, 2
	s_movk_i32 s1, 0x4c
	v_cndmask_b32_e64 v8, 0, 1, vcc
	v_cmp_lt_u32_e32 vcc, 58, v0
	v_mul_lo_u32 v212, v1, s4
	s_movk_i32 s4, 0x62
	v_cndmask_b32_e64 v9, 0, 1, vcc
	v_cmp_lt_u32_e32 vcc, s1, v0
	v_min_u32_e32 v4, 16, v0
	s_movk_i32 s0, 0x42
	v_cndmask_b32_e64 v10, 0, 1, vcc
	v_cmp_lt_u32_e32 vcc, s4, v0
	s_movk_i32 s1, 0x56
	s_movk_i32 s3, 0x70
	v_cndmask_b32_e64 v11, 0, 1, vcc
	v_cmp_lt_u32_e32 vcc, 20, v0
	v_lshlrev_b32_e32 v2, 4, v0
	v_lshlrev_b32_e32 v214, 3, v0
	v_addc_co_u32_e32 v4, vcc, 0, v4, vcc
	v_cmp_lt_u32_e32 vcc, 23, v0
	v_and_b32_e32 v186, 0x70, v2
	v_and_b32_e32 v180, 31, v0
	v_addc_co_u32_e32 v4, vcc, v4, v5, vcc
	v_cmp_lt_u32_e32 vcc, 30, v0
	v_and_b32_e32 v2, 0xc0, v2
	v_and_b32_e32 v5, 0x118, v214
	v_addc_co_u32_e32 v4, vcc, v4, v6, vcc
	v_cmp_lt_u32_e32 vcc, 39, v0
	s_mul_i32 s69, s2, 6
	v_lshrrev_b32_e32 v1, 5, v251
	v_addc_co_u32_e32 v4, vcc, v4, v7, vcc
	v_cmp_lt_u32_e32 vcc, 51, v0
	s_sub_i32 s71, 24, s69
	v_and_b32_e32 v213, 32, v0
	v_addc_co_u32_e32 v4, vcc, v4, v8, vcc
	v_cmp_lt_u32_e32 vcc, s0, v0
	s_add_i32 s0, 0, 0x21000
	v_lshl_add_u32 v217, v0, 2, s0
	v_addc_co_u32_e32 v4, vcc, v4, v9, vcc
	v_cmp_lt_u32_e32 vcc, s1, v0
	s_add_i32 s0, 0, 0x4000
	v_lshlrev_b32_e32 v182, 3, v1
	v_addc_co_u32_e32 v4, vcc, v4, v10, vcc
	v_cmp_lt_u32_e32 vcc, s3, v0
	v_lshlrev_b32_e32 v183, 4, v1
	v_lshlrev_b32_e32 v184, 2, v1
	v_addc_co_u32_e32 v4, vcc, v4, v11, vcc
	v_lshlrev_b32_e32 v215, 3, v4
	v_lshrrev_b32_e32 v4, 1, v0
	v_and_b32_e32 v219, 8, v4
	v_xor_b32_e32 v4, v193, v181
	v_lshlrev_b32_e32 v200, 3, v4
	v_bitop3_b32 v4, v193, v181, 4 bitop3:0x36
	v_lshlrev_b32_e32 v202, 3, v4
	v_lshlrev_b32_e32 v4, 1, v0
	v_and_b32_e32 v4, 32, v4
	v_or3_b32 v220, v4, v2, v5
	v_lshlrev_b32_e32 v2, 2, v180
	v_add_u32_e32 v222, s0, v220
	v_lshl_add_u64 v[204:205], s[12:13], 0, v[2:3]
	v_mul_u32_u24_e32 v2, 0x3440, v193
	s_mov_b32 s0, 0xd100
	v_add3_u32 v224, v2, v202, s0
	s_mul_i32 s0, s2, 48
	s_add_u32 s84, s92, 0x23944800
	s_movk_i32 s94, 0x3440
	v_mad_i32_i24 v226, v1, -4, v180
	v_writelane_b32 v255, s0, 3
	s_mul_i32 s0, s2, 0x300
	v_mbcnt_lo_u32_b32 v1, -1, 0
	s_mov_b32 s43, 0
	v_cmp_gt_u32_e64 s[78:79], 64, v0
	v_add_u32_e32 v201, 0, v186
	v_mov_b32_e32 v187, v3
	v_bfe_u32 v218, v0, 2, 3
	v_or_b32_e32 v221, 4, v193
	v_cmp_gt_u32_e64 s[74:75], 32, v251
	v_lshl_add_u32 v185, v180, 8, 0
	v_mov_b32_e32 v189, v188
	v_and_or_b32 v223, v214, 24, v213
	s_addc_u32 s97, s93, 0
	v_mad_u32_u24 v225, v193, s94, v200
	v_writelane_b32 v255, s0, 4
	s_add_i32 s3, 0, 0x20500
	s_add_i32 s46, 0, 0x20504
	s_movk_i32 s47, 0x1880
	s_mov_b32 s33, 0x800000
	v_mov_b32_e32 v227, 0x6880
	v_mov_b32_e32 v228, 0x1ffffff3
	v_mov_b32_e32 v229, 0xf149f2ca
	v_mbcnt_hi_u32_b32 v230, -1, v1
	v_mov_b32_e32 v231, 0x1880
	s_mov_b32 s100, 0
	s_branch .LBB0_555

.LBB0_555:
	s_barrier
	s_and_saveexec_b64 s[0:1], s[78:79]
	s_cbranch_execz .LBB0_573
	v_mov_b32_e32 v2, 0
	s_mov_b64 s[10:11], exec
	v_readlane_b32 s4, v254, 29
	v_readlane_b32 s5, v254, 30
	s_and_b64 s[4:5], s[10:11], s[4:5]
	s_mov_b64 exec, s[4:5]
	s_cbranch_execz .LBB0_560
	s_mov_b64 s[14:15], exec
	v_mbcnt_lo_u32_b32 v1, s14, 0
	v_mbcnt_hi_u32_b32 v2, s15, v1
	v_cmp_eq_u32_e32 vcc, 0, v2
	s_and_saveexec_b64 s[12:13], vcc
	s_cbranch_execz .LBB0_559
	s_cmp_lg_u32 s100, 0
	s_cbranch_scc1 .Ldq_have
	s_bcnt1_i32_b64 s2, s[14:15]
	v_readlane_b32 s4, v254, 61
	v_mov_b32_e32 v1, s2
	v_readlane_b32 s5, v254, 62
	s_nop 4
	global_atomic_add v4, v3, v1, s[4:5] sc0
	s_branch .LBB0_559
.Ldq_have:
	s_waitcnt vmcnt(0)
	v_mov_b32_e32 v4, v252
.LBB0_559:
	s_or_b64 exec, exec, s[12:13]
	s_waitcnt vmcnt(0)
	v_readfirstlane_b32 s2, v4
	s_nop 1
	v_add_u32_e32 v2, s2, v2

.LBB0_573:
	s_or_b64 exec, exec, s[0:1]
	v_mov_b32_e32 v1, s46
	v_mov_b32_e32 v2, s3
	s_waitcnt lgkmcnt(0)
	s_barrier
	ds_read_b32 v1, v1
	ds_read_b32 v2, v2
	s_mov_b64 s[0:1], -1
	s_waitcnt lgkmcnt(1)
	v_readfirstlane_b32 s40, v1
	s_waitcnt lgkmcnt(0)
	v_cmp_lt_i32_e32 vcc, -1, v2
	v_readfirstlane_b32 s9, v2
	s_cbranch_vccz .LBB0_554
	s_mov_b64 s[10:11], exec
	s_and_b64 s[12:13], s[10:11], s[78:79]
	v_readlane_b32 s14, v254, 29
	v_readlane_b32 s15, v254, 30
	s_and_b64 s[12:13], s[12:13], s[14:15]
	s_mov_b64 exec, s[12:13]
	s_cbranch_execz .Ldq_pfx
	v_mbcnt_lo_u32_b32 v253, s12, 0
	v_mbcnt_hi_u32_b32 v253, s13, v253
	v_cmp_eq_u32_e32 vcc, 0, v253
	s_and_saveexec_b64 s[14:15], vcc
	s_cbranch_execz .Ldq_pfx
	s_bcnt1_i32_b64 s16, s[12:13]
	v_readlane_b32 s18, v254, 61
	v_readlane_b32 s19, v254, 62
	v_mov_b32_e32 v253, s16
	s_nop 4
	global_atomic_add v252, v3, v253, s[18:19] sc0
.Ldq_pfx:
	s_mov_b64 exec, s[10:11]
	s_mov_b32 s100, 1
	s_lshl_b32 s0, s40, 7
	s_add_i32 s2, s9, s0
	v_readlane_b32 s0, v254, 63
	v_readlane_b32 s1, v255, 0
	s_mul_i32 s8, s2, 24
	s_andn2_b64 vcc, exec, s[0:1]
	s_mul_i32 s50, s40, 0x6000
	s_mul_i32 s51, s9, 0xc0
	s_mul_i32 s48, s40, 0x60000
	s_mul_i32 s49, s9, 0xc00
	s_barrier
	s_cbranch_vccnz .LBB0_632
	s_cmpk_gt_i32 s2, 0x2aa
	s_cselect_b64 s[0:1], -1, 0
	s_mov_b64 s[16:17], -1
	s_and_b64 vcc, exec, s[0:1]
	s_mulk_i32 s2, 0xc0
	s_cbranch_vccz .LBB0_577
	v_readlane_b32 s52, v254, 31
	s_add_i32 s4, s8, 0xffffc000
	v_readlane_b32 s56, v254, 35
	v_readlane_b32 s57, v254, 36
	s_lshr_b32 s42, s4, 8
	s_lshl_b32 s4, s9, 10
	v_readlane_b32 s58, v254, 37
	v_readlane_b32 s59, v254, 38
	v_readlane_b32 s60, v254, 39
	v_readlane_b32 s61, v254, 40
	v_readlane_b32 s62, v254, 41
	v_readlane_b32 s63, v254, 42
	v_readlane_b32 s64, v254, 43
	v_readlane_b32 s65, v254, 44
	v_readlane_b32 s66, v254, 45
	v_readlane_b32 s67, v254, 46
	s_mov_b64 s[20:21], s[56:57]
	s_and_b32 s12, s2, 0x780
	s_and_b32 s16, s4, 0x400
	s_lshl_b64 s[14:15], s[42:43], 11
	s_lshl_b64 s[4:5], s[42:43], 24
	s_mov_b64 s[28:29], s[64:65]
	s_add_u32 s4, s28, s4
	s_addc_u32 s5, s29, s5
	s_lshl_b32 s10, s12, 13
	s_add_u32 s4, s4, s10
	s_addc_u32 s5, s5, 0
	s_lshl_b32 s10, s16, 2
	s_add_u32 s10, s4, s10
	v_readlane_b32 s53, v254, 32
	v_readlane_b32 s54, v254, 33
	v_readlane_b32 s55, v254, 34
	s_mov_b64 s[22:23], s[58:59]
	s_mov_b64 s[24:25], s[60:61]
	s_mov_b64 s[26:27], s[62:63]
	s_mov_b64 s[30:31], s[66:67]
	s_mov_b32 s13, s43
	s_addc_u32 s11, s5, 0
	s_or_b32 s14, s14, s16
	s_mov_b64 s[16:17], 0
